# static s_setprio 1 for waves 4-7 at the start of P2 (attention/mLSTM) and P10 (PEER top-k / retrieval); GEMM phases keep their flips
# baseline (speedup 1.0000x reference)
; #define LAS __attribute__((address_space(3)))
; #define SYNC_AFTER(k) do { if (IN(k) && IN((k) + 1)) { GRID_BAR(); } } while (0)
; __device__ __forceinline__ void p2_attention(const Params& P, LAS unsigned char* lds, int lane, int wave, int vb) {
;     const bf16* QKVA = (const bf16*)(P.ws + WS_QKVA); bf16* YA = (bf16*)(P.ws + WS_YA);
;     LAS unsigned char* kbuf = lds + wave * 9728;
;     LAS unsigned char* vbuf = kbuf + 4608;
;     LAS unsigned char* xtab = lds + 8 * 9728;
;     const int qi = lane & 31, h = lane >> 5, lrow = lane >> 3, lch = lane & 7;
;     v4u kr[2][4], vr[2][4]; bf16x8 qb[4];
;     const int u0 = wave * 2, u1 = wave * 2 + 1;
;     if (vb < 512) {
;         const int it0 = attn_item(vb, (int)gridDim.x); const int bh = it0 >> 5, tb = it0 & 31, b = bh >> 3, hh = bh & 7; const bf16* base = QKVA + (size_t)b * SEQ * 1536 + hh * 64; const int t0 = tb * 512 + attn32_qoff(0, u0);
; __global__ void __launch_bounds__(512, 2) mk_fwd(Params P) {
;     ...
;         pg8::gemm_phase<pg8::EpiProj, pg8::StaticOrder, true, true>(lds, g, S, E);
;     }
;     SYNC_AFTER(1);
;     if (IN(2)) { p2_attention(P, lds, lane, wave, vb); __syncthreads(); p2_mlstm_local(P, lds, tid, lane, wave, vb); }
.Lgb1_t_done:
.Lgb1_exit:
.LBB0_345:
	s_or_b64 exec, exec, s[4:5]
	s_waitcnt lgkmcnt(0)
	s_barrier
	v_readfirstlane_b32 s98, v0
	s_nop 3
	s_lshr_b32 s98, s98, 6
	s_cmp_ge_u32 s98, 4
	s_cbranch_scc0 .Lprio_1
	s_setprio 1
.Lprio_1:
.LBB0_346:
	s_cmp_lt_i32 s86, 3
	s_cselect_b64 s[4:5], -1, 0
	s_and_b64 s[28:29], s[4:5], s[2:3]
	s_andn2_b64 vcc, exec, s[28:29]
	s_cbranch_vccnz .LBB0_506
	s_add_u32 s16, s64, 0x9800000
	s_addc_u32 s17, s65, 0
	s_cmpk_gt_i32 s72, 0x1ff
	s_cselect_b64 s[2:3], -1, 0
	v_and_b32_e32 v1, 31, v0
	v_lshrrev_b32_e32 v53, 3, v210
	s_and_b64 vcc, exec, s[2:3]
	s_cbranch_vccnz .LBB0_352
	s_cmpk_lg_i32 s68, 0x100
	s_mov_b32 s4, s72
	s_cbranch_scc1 .LBB0_350
	s_lshl_b32 s0, s72, 1
	s_and_b32 s0, s0, 14
	s_ashr_i32 s1, s72, 8
	s_add_i32 s0, s0, s1
	s_lshl_b32 s0, s0, 5
	s_bfe_u32 s1, s72, 0x50003
	s_or_b32 s4, s0, s1

; #define LAS __attribute__((address_space(3)))
; __device__ __forceinline__ void p10_topk(const Params& P, LAS unsigned char* lds, int tid, int lane, int wave, int vb) {
;     const bf16* Q2 = (const bf16*)(P.ws + WS_Q2); const bf16* K1B = (const bf16*)(P.ws + WS_K1B); const bf16* K2B = (const bf16*)(P.ws + WS_K2B);
;     unsigned char* REC = P.ws + WS_REC; float* GATE = (float*)(P.ws + WS_GATE); const float* SSQ1 = (const float*)(P.ws + WS_SSQ1);
;     LAS bf16* Kl = (LAS bf16*)lds;
;     LAS int* Tb = (LAS int*)(lds + 69632 + wave * 2048);
;     const int r = lane & 15, g = lane >> 4;
;     const int h = vb & 7, wgx = vb >> 3, nwg = gridDim.x >> 3;
;     __syncthreads();
;     for (int i = tid; i < 4096; i += 512) { const int half = i >> 11, rem = i & 2047, n = rem >> 4, c = rem & 15;
;         *(LAS v4u*)(Kl + half * 17408 + n * 136 + c * 8) = *(const v4u*)((half ? K2B : K1B) + (size_t)h * 16384 + n * 128 + c * 8); }
.Lprio_7:
.LBB0_1232:
	s_cmp_lt_i32 s86, 11
	s_cselect_b64 s[0:1], -1, 0
	s_and_b64 s[20:21], s[0:1], s[2:3]
	s_andn2_b64 vcc, exec, s[20:21]
	s_cbranch_vccnz .LBB0_1275
	s_waitcnt vmcnt(0)
	v_mov_b32_e32 v4, v0
	s_movk_i32 s0, 0x1000
	s_and_b32 s18, s72, 7
	v_cmp_gt_i32_e32 vcc, s0, v4
	s_waitcnt lgkmcnt(0)
	s_barrier
	s_and_saveexec_b64 s[2:3], vcc
	s_cbranch_execz .LBB0_1236
	s_lshl_b32 s0, s18, 15
	s_add_u32 s4, s64, s0
	s_addc_u32 s5, s65, 0
	s_add_u32 s4, s4, 0x1680000
	s_addc_u32 s5, s5, 0
	v_lshlrev_b32_e32 v1, 4, v4
	v_lshrrev_b32_e32 v2, 4, v4
	v_and_b32_e32 v3, 15, v4
	v_mul_u32_u24_e32 v2, 0x110, v2
	v_lshl_add_u32 v2, v3, 4, v2
	global_load_dwordx4 v[16:19], v1, s[4:5]
	v_add_u32_e32 v5, 0x2000, v1
	global_load_dwordx4 v[20:23], v5, s[4:5]
	v_add_u32_e32 v6, 0x4000, v1
	global_load_dwordx4 v[24:27], v6, s[4:5]
	v_add_u32_e32 v7, 0x6000, v1
	global_load_dwordx4 v[28:31], v7, s[4:5]
	v_add_u32_e32 v8, 0x40000, v1
	global_load_dwordx4 v[32:35], v8, s[4:5]
	v_add_u32_e32 v9, 0x42000, v1
	global_load_dwordx4 v[36:39], v9, s[4:5]
	v_add_u32_e32 v10, 0x44000, v1
	global_load_dwordx4 v[40:43], v10, s[4:5]
	v_add_u32_e32 v11, 0x46000, v1
	global_load_dwordx4 v[44:47], v11, s[4:5]
	s_waitcnt vmcnt(7)
	ds_write_b128 v2, v[16:19]
	s_waitcnt vmcnt(6)
	ds_write_b128 v2, v[20:23] offset:8704
	s_waitcnt vmcnt(5)
	ds_write_b128 v2, v[24:27] offset:17408
	s_waitcnt vmcnt(4)
	ds_write_b128 v2, v[28:31] offset:26112
	s_waitcnt vmcnt(3)
	ds_write_b128 v2, v[32:35] offset:34816
	s_waitcnt vmcnt(2)
	ds_write_b128 v2, v[36:39] offset:43520
	s_waitcnt vmcnt(1)
	ds_write_b128 v2, v[40:43] offset:52224
	s_waitcnt vmcnt(0)
	ds_write_b128 v2, v[44:47] offset:60928
